# speedup vs baseline: 1.0171x; 1.0097x over previous
_Z7k_finalPKfS0_S0_S0_S0_Pf:
	v_cmp_gt_u32_e32 vcc, 64, v0
	s_cbranch_vccz .Lfin_exit
	s_load_dwordx8 s[4:11], s[0:1], 0x0
	s_load_dwordx4 s[12:15], s[0:1], 0x20
	v_lshlrev_b32_e32 v2, 2, v0
	v_and_b32_e32 v4, 31, v0
	v_lshrrev_b32_e32 v6, 5, v0
	v_lshlrev_b32_e32 v4, 2, v4
	v_lshl_or_b32 v3, v6, 12, v4
	v_lshlrev_b32_e32 v6, 7, v6
	s_waitcnt lgkmcnt(0)
	global_load_dword v10, v2, s[4:5] offset:0
	global_load_dword v11, v2, s[4:5] offset:256
	global_load_dword v12, v2, s[4:5] offset:512
	global_load_dword v13, v2, s[4:5] offset:768
	global_load_dword v14, v2, s[4:5] offset:1024
	global_load_dword v15, v2, s[4:5] offset:1280
	global_load_dword v16, v2, s[4:5] offset:1536
	global_load_dword v17, v2, s[4:5] offset:1792
	global_load_dword v18, v2, s[4:5] offset:2048
	global_load_dword v19, v2, s[4:5] offset:2304
	global_load_dword v20, v2, s[4:5] offset:2560
	global_load_dword v21, v2, s[4:5] offset:2816
	global_load_dword v22, v2, s[4:5] offset:3072
	global_load_dword v23, v2, s[4:5] offset:3328
	global_load_dword v24, v2, s[4:5] offset:3584
	global_load_dword v25, v2, s[4:5] offset:3840
	global_load_dword v30, v3, s[6:7] offset:0
	global_load_dword v31, v3, s[6:7] offset:128
	global_load_dword v32, v3, s[6:7] offset:256
	global_load_dword v33, v3, s[6:7] offset:384
	global_load_dword v34, v3, s[6:7] offset:512
	global_load_dword v35, v3, s[6:7] offset:640
	global_load_dword v36, v3, s[6:7] offset:768
	global_load_dword v37, v3, s[6:7] offset:896
	global_load_dword v38, v3, s[6:7] offset:1024
	global_load_dword v39, v3, s[6:7] offset:1152
	global_load_dword v40, v3, s[6:7] offset:1280
	global_load_dword v41, v3, s[6:7] offset:1408
	global_load_dword v42, v3, s[6:7] offset:1536
	global_load_dword v43, v3, s[6:7] offset:1664
	global_load_dword v44, v3, s[6:7] offset:1792
	global_load_dword v45, v3, s[6:7] offset:1920
	global_load_dword v46, v3, s[6:7] offset:2048
	global_load_dword v47, v3, s[6:7] offset:2176
	global_load_dword v48, v3, s[6:7] offset:2304
	global_load_dword v49, v3, s[6:7] offset:2432
	global_load_dword v50, v3, s[6:7] offset:2560
	global_load_dword v51, v3, s[6:7] offset:2688
	global_load_dword v52, v3, s[6:7] offset:2816
	global_load_dword v53, v3, s[6:7] offset:2944
	global_load_dword v54, v3, s[6:7] offset:3072
	global_load_dword v55, v3, s[6:7] offset:3200
	global_load_dword v56, v3, s[6:7] offset:3328
	global_load_dword v57, v3, s[6:7] offset:3456
	global_load_dword v58, v3, s[6:7] offset:3584
	global_load_dword v59, v3, s[6:7] offset:3712
	global_load_dword v60, v3, s[6:7] offset:3840
	global_load_dword v61, v3, s[6:7] offset:3968
	global_load_dword v62, v4, s[8:9]
	global_load_dword v63, v4, s[10:11]
	s_load_dword s16, s[12:13], 0x0
	s_waitcnt vmcnt(34)
	v_add_f32_e32 v5, v10, v11
	v_add_f32_e32 v5, v5, v12
	v_add_f32_e32 v5, v5, v13
	v_add_f32_e32 v5, v5, v14
	v_add_f32_e32 v5, v5, v15
	v_add_f32_e32 v5, v5, v16
	v_add_f32_e32 v5, v5, v17
	v_add_f32_e32 v5, v5, v18
	v_add_f32_e32 v5, v5, v19
	v_add_f32_e32 v5, v5, v20
	v_add_f32_e32 v5, v5, v21
	v_add_f32_e32 v5, v5, v22
	v_add_f32_e32 v5, v5, v23
	v_add_f32_e32 v5, v5, v24
	v_add_f32_e32 v5, v5, v25
	v_mul_f32_e32 v5, 0x3727c5ac, v5
	ds_write_b32 v2, v5
	ds_read_b128 v[64:67], v6 offset:0
	ds_read_b128 v[68:71], v6 offset:16
	ds_read_b128 v[72:75], v6 offset:32
	ds_read_b128 v[76:79], v6 offset:48
	ds_read_b128 v[80:83], v6 offset:64
	ds_read_b128 v[84:87], v6 offset:80
	ds_read_b128 v[88:91], v6 offset:96
	ds_read_b128 v[92:95], v6 offset:112
	s_waitcnt vmcnt(0) lgkmcnt(0)
	v_mul_f32_e32 v7, v64, v30
	v_fmac_f32_e32 v7, v65, v31
	v_fmac_f32_e32 v7, v66, v32
	v_fmac_f32_e32 v7, v67, v33
	v_fmac_f32_e32 v7, v68, v34
	v_fmac_f32_e32 v7, v69, v35
	v_fmac_f32_e32 v7, v70, v36
	v_fmac_f32_e32 v7, v71, v37
	v_fmac_f32_e32 v7, v72, v38
	v_fmac_f32_e32 v7, v73, v39
	v_fmac_f32_e32 v7, v74, v40
	v_fmac_f32_e32 v7, v75, v41
	v_fmac_f32_e32 v7, v76, v42
	v_fmac_f32_e32 v7, v77, v43
	v_fmac_f32_e32 v7, v78, v44
	v_fmac_f32_e32 v7, v79, v45
	v_fmac_f32_e32 v7, v80, v46
	v_fmac_f32_e32 v7, v81, v47
	v_fmac_f32_e32 v7, v82, v48
	v_fmac_f32_e32 v7, v83, v49
	v_fmac_f32_e32 v7, v84, v50
	v_fmac_f32_e32 v7, v85, v51
	v_fmac_f32_e32 v7, v86, v52
	v_fmac_f32_e32 v7, v87, v53
	v_fmac_f32_e32 v7, v88, v54
	v_fmac_f32_e32 v7, v89, v55
	v_fmac_f32_e32 v7, v90, v56
	v_fmac_f32_e32 v7, v91, v57
	v_fmac_f32_e32 v7, v92, v58
	v_fmac_f32_e32 v7, v93, v59
	v_fmac_f32_e32 v7, v94, v60
	v_fmac_f32_e32 v7, v95, v61
	v_mov_b32_e32 v8, v7
	s_nop 1
	v_permlane32_swap_b32 v7, v8
	v_add_f32_e32 v7, v7, v8
	v_add_f32_e32 v7, v7, v62
	v_max_f32_e32 v7, 0, v7
	v_mul_f32_e32 v7, v7, v63
	s_nop 1
	v_add_f32_dpp v7, v7, v7 quad_perm:[1,0,3,2] row_mask:0xf bank_mask:0xf
	s_nop 1
	v_add_f32_dpp v7, v7, v7 quad_perm:[2,3,0,1] row_mask:0xf bank_mask:0xf
	s_nop 1
	v_add_f32_dpp v7, v7, v7 row_half_mirror row_mask:0xf bank_mask:0xf
	s_nop 1
	v_add_f32_dpp v7, v7, v7 row_mirror row_mask:0xf bank_mask:0xf
	v_mov_b32_e32 v8, v7
	s_nop 1
	v_permlane16_swap_b32 v7, v8
	v_add_f32_e32 v7, v7, v8
	v_add_f32_e32 v7, s16, v7
	v_mul_f32_e32 v7, 0xbfb8aa3b, v7
	v_exp_f32_e32 v7, v7
	s_nop 0
	v_add_f32_e32 v7, 1.0, v7
	v_rcp_f32_e32 v7, v7
	v_cmp_eq_u32_e32 vcc, 0, v0
	s_and_saveexec_b64 s[2:3], vcc
	v_mov_b32_e32 v9, 0
	global_store_dword v9, v7, s[14:15]

	.amdhsa_kernel _Z7k_finalPKfS0_S0_S0_S0_Pf
		.amdhsa_group_segment_fixed_size 1408
		.amdhsa_private_segment_fixed_size 0
		.amdhsa_kernarg_size 48
		.amdhsa_user_sgpr_count 2
		.amdhsa_user_sgpr_dispatch_ptr 0
		.amdhsa_user_sgpr_queue_ptr 0
		.amdhsa_user_sgpr_kernarg_segment_ptr 1
		.amdhsa_user_sgpr_dispatch_id 0
		.amdhsa_user_sgpr_kernarg_preload_length 0
		.amdhsa_user_sgpr_kernarg_preload_offset 0
		.amdhsa_user_sgpr_private_segment_size 0
		.amdhsa_uses_dynamic_stack 0
		.amdhsa_enable_private_segment 0
		.amdhsa_system_sgpr_workgroup_id_x 1
		.amdhsa_system_sgpr_workgroup_id_y 0
		.amdhsa_system_sgpr_workgroup_id_z 0
		.amdhsa_system_sgpr_workgroup_info 0
		.amdhsa_system_vgpr_workitem_id 0
		.amdhsa_next_free_vgpr 96
		.amdhsa_next_free_sgpr 20
		.amdhsa_accum_offset 96
		.amdhsa_reserve_vcc 1
		.amdhsa_float_round_mode_32 0
		.amdhsa_float_round_mode_16_64 0
		.amdhsa_float_denorm_mode_32 3
		.amdhsa_float_denorm_mode_16_64 3
		.amdhsa_dx10_clamp 1
		.amdhsa_ieee_mode 1
		.amdhsa_fp16_overflow 0
		.amdhsa_tg_split 0
		.amdhsa_exception_fp_ieee_invalid_op 0
		.amdhsa_exception_fp_denorm_src 0
		.amdhsa_exception_fp_ieee_div_zero 0
		.amdhsa_exception_fp_ieee_overflow 0
		.amdhsa_exception_fp_ieee_underflow 0
		.amdhsa_exception_fp_ieee_inexact 0
		.amdhsa_exception_int_div_zero 0
	.end_amdhsa_kernel

_Z7k_layerILi1EEvPKiS1_PKfS3_PKDF16_S3_S5_S5_PDF16_P15HIP_vector_typeIfLj4EES9_S3_S3_S3_S3_S3_S3_PfSA_:
	s_setprio 1
	s_load_dwordx8 s[8:15], s[0:1], 0x38
	s_load_dwordx8 s[16:23], s[0:1], 0x0
	s_load_dwordx2 s[24:25], s[0:1], 0x20
	s_movk_i32 s3, 0x200
	v_readfirstlane_b32 s53, v0
	v_cmp_gt_u32_e32 vcc, s3, v0
	s_and_saveexec_b64 s[4:5], vcc
	s_cbranch_execz .LBB6_3
	s_load_dwordx4 s[28:31], s[0:1], 0x58
	v_lshlrev_b32_e32 v93, 2, v0
	s_waitcnt lgkmcnt(0)
	global_load_dword v95, v93, s[28:29]
	global_load_dword v94, v93, s[30:31]
	v_add_u32_e32 v93, 0x4a00, v93

.LBB6_91:
	s_setprio 0
	s_lshl_b32 s0, s52, 5
	s_mov_b32 s1, 0
	s_lshl_b64 s[0:1], s[0:1], 10
	s_add_u32 s2, s8, s0
	s_addc_u32 s3, s9, s1
	v_lshlrev_b32_e32 v34, 4, v1
	global_load_dwordx4 v[2:5], v34, s[2:3]
	global_load_dwordx4 v[18:21], v34, s[2:3] offset:1024
	global_load_dwordx4 v[22:25], v34, s[2:3] offset:2048
	v_mov_b32_e32 v35, 0
	s_movk_i32 s0, 0x1000
	v_lshl_add_u64 v[36:37], s[2:3], 0, v[34:35]
	v_add_co_u32_e32 v6, vcc, s0, v36
	s_movk_i32 s1, 0x210
	s_movk_i32 s4, 0x2000
	v_addc_co_u32_e32 v7, vcc, 0, v37, vcc
	v_mad_u32_u24 v82, v78, s1, v87
	v_add_co_u32_e32 v62, vcc, s4, v36
	s_nop 1
	v_addc_co_u32_e32 v63, vcc, 0, v37, vcc
	global_load_dwordx4 v[26:29], v34, s[2:3] offset:3072
	global_load_dwordx4 v[30:33], v[62:63], off offset:-4096
	global_load_dwordx4 v[38:41], v[6:7], off offset:1024
	global_load_dwordx4 v[42:45], v[6:7], off offset:2048
	global_load_dwordx4 v[46:49], v[6:7], off offset:3072
	s_waitcnt lgkmcnt(0)
	s_barrier
	ds_read_b128 v[6:9], v82
	ds_read_b128 v[50:53], v82 offset:32
	s_waitcnt vmcnt(7) lgkmcnt(1)
	v_mfma_f32_32x32x16_f16 v[2:17], v[2:5], v[6:9], 0
	s_waitcnt vmcnt(6) lgkmcnt(0)
	v_mfma_f32_32x32x16_f16 v[2:17], v[18:21], v[50:53], v[2:17]
	ds_read_b128 v[18:21], v82 offset:64
	global_load_dwordx4 v[50:53], v[62:63], off
	global_load_dwordx4 v[54:57], v[62:63], off offset:1024
	ds_read_b128 v[58:61], v82 offset:96
	s_waitcnt vmcnt(7) lgkmcnt(1)
	v_mfma_f32_32x32x16_f16 v[2:17], v[22:25], v[18:21], v[2:17]
	global_load_dwordx4 v[18:21], v[62:63], off offset:2048
	global_load_dwordx4 v[22:25], v[62:63], off offset:3072
	s_waitcnt vmcnt(8) lgkmcnt(0)
	v_mfma_f32_32x32x16_f16 v[2:17], v[26:29], v[58:61], v[2:17]
	ds_read_b128 v[26:29], v82 offset:128
	ds_read_b128 v[58:61], v82 offset:160
	s_movk_i32 s0, 0x3000
	s_movk_i32 s2, 0x4000
	s_waitcnt vmcnt(7) lgkmcnt(1)
	v_mfma_f32_32x32x16_f16 v[2:17], v[30:33], v[26:29], v[2:17]
	ds_read_b128 v[26:29], v82 offset:192
	ds_read_b128 v[30:33], v82 offset:224
	s_waitcnt vmcnt(6) lgkmcnt(2)
	v_mfma_f32_32x32x16_f16 v[2:17], v[38:41], v[58:61], v[2:17]
	v_add_co_u32_e32 v58, vcc, s0, v36
	s_nop 1
	v_addc_co_u32_e32 v59, vcc, 0, v37, vcc
	v_add_co_u32_e32 v66, vcc, s2, v36
	s_waitcnt vmcnt(5) lgkmcnt(1)
	v_mfma_f32_32x32x16_f16 v[2:17], v[42:45], v[26:29], v[2:17]
	v_addc_co_u32_e32 v67, vcc, 0, v37, vcc
	global_load_dwordx4 v[26:29], v[58:59], off offset:1024
	global_load_dwordx4 v[38:41], v[58:59], off offset:2048
	global_load_dwordx4 v[42:45], v[66:67], off offset:-4096
	s_nop 0
	global_load_dwordx4 v[58:61], v[58:59], off offset:3072
	s_waitcnt vmcnt(8) lgkmcnt(0)
	v_mfma_f32_32x32x16_f16 v[2:17], v[46:49], v[30:33], v[2:17]
	ds_read_b128 v[30:33], v82 offset:256
	ds_read_b128 v[46:49], v82 offset:288
	s_waitcnt vmcnt(7) lgkmcnt(1)
	v_mfma_f32_32x32x16_f16 v[2:17], v[50:53], v[30:33], v[2:17]
	ds_read_b128 v[30:33], v82 offset:320
	s_waitcnt vmcnt(6) lgkmcnt(1)
	v_mfma_f32_32x32x16_f16 v[2:17], v[54:57], v[46:49], v[2:17]
	global_load_dwordx4 v[46:49], v[66:67], off
	global_load_dwordx4 v[50:53], v[66:67], off offset:1024
	ds_read_b128 v[54:57], v82 offset:352
	global_load_dwordx4 v[62:65], v[66:67], off offset:2048
	s_nop 0
	global_load_dwordx4 v[66:69], v[66:67], off offset:3072
	s_waitcnt vmcnt(9) lgkmcnt(1)
	v_mfma_f32_32x32x16_f16 v[2:17], v[18:21], v[30:33], v[2:17]
	s_waitcnt vmcnt(8) lgkmcnt(0)
	v_mfma_f32_32x32x16_f16 v[2:17], v[22:25], v[54:57], v[2:17]
	ds_read_b128 v[18:21], v82 offset:384
	ds_read_b128 v[22:25], v82 offset:416
	s_movk_i32 s0, 0x5000
	s_movk_i32 s2, 0x6000
	s_waitcnt vmcnt(5) lgkmcnt(1)
	v_mfma_f32_32x32x16_f16 v[2:17], v[42:45], v[18:21], v[2:17]
	s_waitcnt lgkmcnt(0)
	v_mfma_f32_32x32x16_f16 v[2:17], v[26:29], v[22:25], v[2:17]
	ds_read_b128 v[18:21], v82 offset:448
	ds_read_b128 v[22:25], v82 offset:480
	v_add_co_u32_e32 v26, vcc, s0, v36
	s_nop 1
	v_addc_co_u32_e32 v27, vcc, 0, v37, vcc
	v_add_co_u32_e32 v80, vcc, s2, v36
	s_waitcnt lgkmcnt(1)
	v_mfma_f32_32x32x16_f16 v[2:17], v[38:41], v[18:21], v[2:17]
	v_addc_co_u32_e32 v81, vcc, 0, v37, vcc
	global_load_dwordx4 v[38:41], v[26:27], off offset:1024
	global_load_dwordx4 v[42:45], v[26:27], off offset:2048
	global_load_dwordx4 v[54:57], v[80:81], off offset:-4096
	global_load_dwordx4 v[70:73], v[26:27], off offset:3072
	s_waitcnt vmcnt(8) lgkmcnt(0)
	v_mfma_f32_32x32x16_f16 v[2:17], v[58:61], v[22:25], v[2:17]
	ds_read_b128 v[18:21], v82
	ds_read_b128 v[58:61], v82 offset:32
	s_waitcnt vmcnt(7) lgkmcnt(1)
	v_mfma_f32_32x32x16_f16 v[18:33], v[46:49], v[18:21], 0
	ds_read_b128 v[46:49], v82 offset:64
	s_waitcnt vmcnt(6) lgkmcnt(1)
	v_mfma_f32_32x32x16_f16 v[18:33], v[50:53], v[58:61], v[18:33]
	global_load_dwordx4 v[50:53], v[80:81], off
	global_load_dwordx4 v[58:61], v[80:81], off offset:1024
	ds_read_b128 v[74:77], v82 offset:96
	s_waitcnt vmcnt(7) lgkmcnt(1)
	v_mfma_f32_32x32x16_f16 v[18:33], v[62:65], v[46:49], v[18:33]
	global_load_dwordx4 v[46:49], v[80:81], off offset:2048
	global_load_dwordx4 v[62:65], v[80:81], off offset:3072
	s_waitcnt vmcnt(8) lgkmcnt(0)
	v_mfma_f32_32x32x16_f16 v[18:33], v[66:69], v[74:77], v[18:33]
	ds_read_b128 v[66:69], v82 offset:128
	ds_read_b128 v[74:77], v82 offset:160
	s_movk_i32 s0, 0x7000
	v_add_co_u32_e32 v80, vcc, s0, v36
	s_waitcnt vmcnt(5) lgkmcnt(1)
	v_mfma_f32_32x32x16_f16 v[18:33], v[54:57], v[66:69], v[18:33]
	v_addc_co_u32_e32 v81, vcc, 0, v37, vcc
	s_waitcnt lgkmcnt(0)
	v_mfma_f32_32x32x16_f16 v[18:33], v[38:41], v[74:77], v[18:33]
	ds_read_b128 v[38:41], v82 offset:192
	ds_read_b128 v[54:57], v82 offset:224
	global_load_dwordx4 v[66:69], v[80:81], off
	global_load_dwordx4 v[74:77], v[80:81], off offset:1024
	s_waitcnt lgkmcnt(1)
	v_mfma_f32_32x32x16_f16 v[18:33], v[42:45], v[38:41], v[18:33]
	global_load_dwordx4 v[36:39], v[80:81], off offset:2048
	global_load_dwordx4 v[40:43], v[80:81], off offset:3072
	s_waitcnt vmcnt(8) lgkmcnt(0)
	v_mfma_f32_32x32x16_f16 v[18:33], v[70:73], v[54:57], v[18:33]
	ds_read_b128 v[54:57], v82 offset:256
	ds_read_b128 v[70:73], v82 offset:288
	s_waitcnt vmcnt(7) lgkmcnt(1)
	v_mfma_f32_32x32x16_f16 v[18:33], v[50:53], v[54:57], v[18:33]
	ds_read_b128 v[50:53], v82 offset:320
	ds_read_b128 v[54:57], v82 offset:352
	s_waitcnt vmcnt(6) lgkmcnt(2)
	v_mfma_f32_32x32x16_f16 v[18:33], v[58:61], v[70:73], v[18:33]
	s_waitcnt vmcnt(5) lgkmcnt(1)
	v_mfma_f32_32x32x16_f16 v[18:33], v[46:49], v[50:53], v[18:33]
	s_waitcnt vmcnt(4) lgkmcnt(0)
	v_mfma_f32_32x32x16_f16 v[18:33], v[62:65], v[54:57], v[18:33]
	ds_read_b128 v[44:47], v82 offset:384
	ds_read_b128 v[48:51], v82 offset:416
	s_waitcnt vmcnt(3) lgkmcnt(1)
	v_mfma_f32_32x32x16_f16 v[18:33], v[66:69], v[44:47], v[18:33]
	s_waitcnt vmcnt(2) lgkmcnt(0)
	v_mfma_f32_32x32x16_f16 v[18:33], v[74:77], v[48:51], v[18:33]
	ds_read_b128 v[44:47], v82 offset:448
	ds_read_b128 v[48:51], v82 offset:480
	s_waitcnt vmcnt(1) lgkmcnt(1)
	v_mfma_f32_32x32x16_f16 v[18:33], v[36:39], v[44:47], v[18:33]
	s_waitcnt vmcnt(0) lgkmcnt(0)
	v_mfma_f32_32x32x16_f16 v[18:33], v[40:43], v[48:51], v[18:33]
	s_and_b32 s0, s53, 0xffffffc0
	v_or_b32_e32 v34, s0, v79
	v_lshlrev_b32_e32 v48, 2, v34
	s_barrier
	ds_read_b128 v[36:39], v48 offset:18944
	ds_read_b128 v[40:43], v48 offset:18976
	ds_read_b128 v[44:47], v48 offset:19968
	v_cmp_lt_u32_e32 vcc, 31, v1
	s_waitcnt lgkmcnt(2)
	v_mul_f32_e32 v37, v3, v37
	v_fmac_f32_e32 v37, v2, v36
	v_fmac_f32_e32 v37, v4, v38
	v_fmac_f32_e32 v37, v5, v39
	s_waitcnt lgkmcnt(0)
	v_mul_f32_e32 v45, v3, v45
	v_add_f32_e32 v49, 0, v37
	ds_read_b128 v[36:39], v48 offset:20000
	v_fmac_f32_e32 v45, v2, v44
	v_cvt_pk_f16_f32 v44, v2, v3
	v_lshlrev_b32_e32 v2, 1, v34
	v_mad_u32_u24 v34, v78, s1, v2
	v_mul_f32_e32 v2, v7, v41
	v_fmac_f32_e32 v2, v6, v40
	v_fmac_f32_e32 v2, v8, v42
	v_fmac_f32_e32 v2, v9, v43
	v_add_f32_e32 v40, v49, v2
	s_waitcnt lgkmcnt(0)
	v_mul_f32_e32 v2, v7, v37
	v_fmac_f32_e32 v45, v4, v46
	v_fmac_f32_e32 v2, v6, v36
	v_fmac_f32_e32 v45, v5, v47
	v_fmac_f32_e32 v2, v8, v38
	v_add_f32_e32 v46, 0, v45
	v_fmac_f32_e32 v2, v9, v39
	v_cvt_pk_f16_f32 v45, v4, v5
	v_add_f32_e32 v41, v46, v2
	ds_read_b128 v[2:5], v48 offset:19008
	v_cvt_pk_f16_f32 v9, v8, v9
	v_cvt_pk_f16_f32 v8, v6, v7
	ds_write2_b64 v34, v[44:45], v[8:9] offset1:2
	ds_read_b128 v[6:9], v48 offset:20032
	ds_read_b128 v[36:39], v48 offset:19040
	s_waitcnt lgkmcnt(3)
	v_mul_f32_e32 v3, v11, v3
	v_fmac_f32_e32 v3, v10, v2
	v_fmac_f32_e32 v3, v12, v4
	v_fmac_f32_e32 v3, v13, v5
	v_add_f32_e32 v40, v40, v3
	ds_read_b128 v[2:5], v48 offset:20064
	s_waitcnt lgkmcnt(2)
	v_mul_f32_e32 v7, v11, v7
	v_fmac_f32_e32 v7, v10, v6
	v_fmac_f32_e32 v7, v12, v8
	v_fmac_f32_e32 v7, v13, v9
	s_waitcnt lgkmcnt(0)
	v_mul_f32_e32 v3, v15, v3
	v_fmac_f32_e32 v3, v14, v2
	v_fmac_f32_e32 v3, v16, v4
	v_add_f32_e32 v8, v41, v7
	v_fmac_f32_e32 v3, v17, v5
	v_mul_f32_e32 v9, v15, v37
	v_add_f32_e32 v37, v8, v3
	ds_read_b128 v[2:5], v48 offset:19072
	v_fmac_f32_e32 v9, v14, v36
	v_fmac_f32_e32 v9, v16, v38
	v_fmac_f32_e32 v9, v17, v39
	v_cvt_pk_f16_f32 v7, v12, v13
	s_waitcnt lgkmcnt(0)
	v_mul_f32_e32 v3, v19, v3
	v_fmac_f32_e32 v3, v18, v2
	v_cvt_pk_f16_f32 v6, v10, v11
	v_add_f32_e32 v36, v40, v9
	v_cvt_pk_f16_f32 v9, v16, v17
	v_cvt_pk_f16_f32 v8, v14, v15
	v_fmac_f32_e32 v3, v20, v4
	ds_write2_b64 v34, v[6:7], v[8:9] offset0:4 offset1:6
	v_fmac_f32_e32 v3, v21, v5
	ds_read_b128 v[6:9], v48 offset:20096
	ds_read_b128 v[10:13], v48 offset:19104
	v_add_f32_e32 v14, v36, v3
	ds_read_b128 v[2:5], v48 offset:20128
	s_waitcnt lgkmcnt(2)
	v_mul_f32_e32 v7, v19, v7
	v_fmac_f32_e32 v7, v18, v6
	v_fmac_f32_e32 v7, v20, v8
	s_waitcnt lgkmcnt(0)
	v_mul_f32_e32 v3, v23, v3
	v_fmac_f32_e32 v3, v22, v2
	v_fmac_f32_e32 v7, v21, v9
	v_fmac_f32_e32 v3, v24, v4
	v_add_f32_e32 v8, v37, v7
	v_fmac_f32_e32 v3, v25, v5
	v_add_f32_e32 v15, v8, v3
	ds_read_b128 v[2:5], v48 offset:19136
	v_mul_f32_e32 v9, v23, v11
	v_fmac_f32_e32 v9, v22, v10
	v_fmac_f32_e32 v9, v24, v12
	v_fmac_f32_e32 v9, v25, v13
	s_waitcnt lgkmcnt(0)
	v_mul_f32_e32 v3, v27, v3
	v_cvt_pk_f16_f32 v7, v20, v21
	v_cvt_pk_f16_f32 v6, v18, v19
	v_add_f32_e32 v14, v14, v9
	v_cvt_pk_f16_f32 v9, v24, v25
	v_cvt_pk_f16_f32 v8, v22, v23
	v_fmac_f32_e32 v3, v26, v2
	ds_write2_b64 v34, v[6:7], v[8:9] offset0:8 offset1:10
	v_fmac_f32_e32 v3, v28, v4
	ds_read_b128 v[6:9], v48 offset:19168
	ds_read_b128 v[10:13], v48 offset:20160
	v_fmac_f32_e32 v3, v29, v5
	v_add_f32_e32 v14, v14, v3
	ds_read_b128 v[2:5], v48 offset:20192
	s_waitcnt lgkmcnt(2)
	v_mul_f32_e32 v7, v31, v7
	s_waitcnt lgkmcnt(1)
	v_mul_f32_e32 v11, v27, v11
	v_fmac_f32_e32 v11, v26, v10
	v_fmac_f32_e32 v11, v28, v12
	s_waitcnt lgkmcnt(0)
	v_mul_f32_e32 v3, v31, v3
	v_fmac_f32_e32 v3, v30, v2
	v_fmac_f32_e32 v11, v29, v13
	v_fmac_f32_e32 v7, v30, v6
	v_fmac_f32_e32 v3, v32, v4
	v_add_f32_e32 v12, v15, v11
	v_fmac_f32_e32 v7, v32, v8
	v_fmac_f32_e32 v3, v33, v5
	v_cvt_pk_f16_f32 v11, v28, v29
	v_cvt_pk_f16_f32 v10, v26, v27
	v_fmac_f32_e32 v7, v33, v9
	v_add_f32_e32 v4, v12, v3
	v_cvt_pk_f16_f32 v3, v32, v33
	v_cvt_pk_f16_f32 v2, v30, v31
	v_add_f32_e32 v6, v14, v7
	ds_write2_b64 v34, v[10:11], v[2:3] offset0:12 offset1:14
	v_or_b32_e32 v3, s33, v78
	s_nop 1
	v_permlane32_swap_b32 v6, v4
	v_lshl_add_u32 v34, v3, 2, s52
	v_add_f32_e32 v2, v6, v4
	s_and_saveexec_b64 s[2:3], vcc
	s_xor_b64 s[2:3], exec, s[2:3]
	s_cbranch_execz .LBB6_93
	v_lshl_add_u64 v[4:5], v[34:35], 2, s[14:15]
	global_store_dword v[4:5], v2, off

_Z7k_layerILi2EEvPKiS1_PKfS3_PKDF16_S3_S5_S5_PDF16_P15HIP_vector_typeIfLj4EES9_S3_S3_S3_S3_S3_S3_PfSA_:
	s_setprio 1
	s_load_dwordx8 s[20:27], s[0:1], 0x0
	s_load_dwordx2 s[28:29], s[0:1], 0x20
	s_and_b32 s7, s2, 7
	s_cmp_gt_u32 s7, 4
	v_readfirstlane_b32 s3, v0
	s_cbranch_scc0 .LBB7_2
	s_mul_i32 s4, s7, 0x186
	s_add_i32 s6, s4, 5
	s_mov_b64 s[4:5], 0
	s_branch .LBB7_3

.LBB7_91:
	s_setprio 0
	s_movk_i32 s0, 0x100
	v_cmp_gt_u32_e32 vcc, s0, v0
	s_waitcnt lgkmcnt(0)
	s_barrier
	s_and_saveexec_b64 s[0:1], vcc
	s_cbranch_execz .LBB7_96
	v_and_b32_e32 v8, 7, v0
	v_lshlrev_b32_e32 v6, 4, v8
	global_load_dwordx4 v[2:5], v6, s[12:13]
	v_mov_b32_e32 v7, 0
	v_mul_u32_u24_e32 v9, 0x110, v1
	v_lshl_add_u64 v[6:7], s[10:11], 0, v[6:7]
	s_mov_b64 s[4:5], 0

amdhsa.kernels:
  - .agpr_count:     0
    .args:
      - .actual_access:  read_only
        .address_space:  global
        .offset:         0
        .size:           8
        .value_kind:     global_buffer
      - .actual_access:  write_only
        .address_space:  global
        .offset:         8
        .size:           8
        .value_kind:     global_buffer
      - .actual_access:  read_only
        .address_space:  global
        .offset:         16
        .size:           8
        .value_kind:     global_buffer
      - .actual_access:  read_only
        .address_space:  global
        .offset:         24
        .size:           8
        .value_kind:     global_buffer
      - .actual_access:  read_only
        .address_space:  global
        .offset:         32
        .size:           8
        .value_kind:     global_buffer
      - .actual_access:  read_only
        .address_space:  global
        .offset:         40
        .size:           8
        .value_kind:     global_buffer
      - .actual_access:  read_only
        .address_space:  global
        .offset:         48
        .size:           8
        .value_kind:     global_buffer
      - .actual_access:  read_only
        .address_space:  global
        .offset:         56
        .size:           8
        .value_kind:     global_buffer
      - .actual_access:  read_only
        .address_space:  global
        .offset:         64
        .size:           8
        .value_kind:     global_buffer
      - .actual_access:  read_only
        .address_space:  global
        .offset:         72
        .size:           8
        .value_kind:     global_buffer
      - .actual_access:  read_only
        .address_space:  global
        .offset:         80
        .size:           8
        .value_kind:     global_buffer
      - .actual_access:  write_only
        .address_space:  global
        .offset:         88
        .size:           8
        .value_kind:     global_buffer
      - .actual_access:  write_only
        .address_space:  global
        .offset:         96
        .size:           8
        .value_kind:     global_buffer
      - .actual_access:  write_only
        .address_space:  global
        .offset:         104
        .size:           8
        .value_kind:     global_buffer
      - .actual_access:  write_only
        .address_space:  global
        .offset:         112
        .size:           8
        .value_kind:     global_buffer
      - .actual_access:  write_only
        .address_space:  global
        .offset:         120
        .size:           8
        .value_kind:     global_buffer
    .group_segment_fixed_size: 1564
    .kernarg_segment_align: 8
    .kernarg_segment_size: 128
    .language:       OpenCL C
    .language_version:
      - 2
      - 0
    .max_flat_workgroup_size: 1024
    .name:           _Z6k_pre1PKiPiPKfS3_S3_S3_S3_S3_S3_S3_S3_PDF16_S4_S4_PfS5_
    .private_segment_fixed_size: 0
    .sgpr_count:     26
    .sgpr_spill_count: 0
    .symbol:         _Z6k_pre1PKiPiPKfS3_S3_S3_S3_S3_S3_S3_S3_PDF16_S4_S4_PfS5_.kd
    .uniform_work_group_size: 1
    .uses_dynamic_stack: false
    .vgpr_count:     64
    .vgpr_spill_count: 0
    .wavefront_size: 64
  - .agpr_count:     0
    .args:
      - .actual_access:  read_only
        .address_space:  global
        .offset:         0
        .size:           8
        .value_kind:     global_buffer
      - .actual_access:  read_only
        .address_space:  global
        .offset:         8
        .size:           8
        .value_kind:     global_buffer
      - .actual_access:  read_only
        .address_space:  global
        .offset:         16
        .size:           8
        .value_kind:     global_buffer
      - .actual_access:  read_only
        .address_space:  global
        .offset:         24
        .size:           8
        .value_kind:     global_buffer
      - .actual_access:  write_only
        .address_space:  global
        .offset:         32
        .size:           8
        .value_kind:     global_buffer
      - .actual_access:  write_only
        .address_space:  global
        .offset:         40
        .size:           8
        .value_kind:     global_buffer
    .group_segment_fixed_size: 1632
    .kernarg_segment_align: 8
    .kernarg_segment_size: 48
    .language:       OpenCL C
    .language_version:
      - 2
      - 0
    .max_flat_workgroup_size: 1024
    .name:           _Z9k_scatterPKiS0_S0_S0_PiS1_
    .private_segment_fixed_size: 0
    .sgpr_count:     22
    .sgpr_spill_count: 0
    .symbol:         _Z9k_scatterPKiS0_S0_S0_PiS1_.kd
    .uniform_work_group_size: 1
    .uses_dynamic_stack: false
    .vgpr_count:     50
    .vgpr_spill_count: 0
    .wavefront_size: 64
  - .agpr_count:     0
    .args:
      - .actual_access:  read_only
        .address_space:  global
        .offset:         0
        .size:           8
        .value_kind:     global_buffer
      - .actual_access:  read_only
        .address_space:  global
        .offset:         8
        .size:           8
        .value_kind:     global_buffer
      - .actual_access:  write_only
        .address_space:  global
        .offset:         16
        .size:           8
        .value_kind:     global_buffer
      - .actual_access:  write_only
        .address_space:  global
        .offset:         24
        .size:           8
        .value_kind:     global_buffer
      - .actual_access:  read_only
        .address_space:  global
        .offset:         32
        .size:           8
        .value_kind:     global_buffer
      - .actual_access:  read_only
        .address_space:  global
        .offset:         40
        .size:           8
        .value_kind:     global_buffer
      - .actual_access:  read_only
        .address_space:  global
        .offset:         48
        .size:           8
        .value_kind:     global_buffer
      - .actual_access:  read_only
        .address_space:  global
        .offset:         56
        .size:           8
        .value_kind:     global_buffer
      - .actual_access:  write_only
        .address_space:  global
        .offset:         64
        .size:           8
        .value_kind:     global_buffer
      - .actual_access:  write_only
        .address_space:  global
        .offset:         72
        .size:           8
        .value_kind:     global_buffer
      - .actual_access:  write_only
        .address_space:  global
        .offset:         80
        .size:           8
        .value_kind:     global_buffer
    .group_segment_fixed_size: 38720
    .kernarg_segment_align: 8
    .kernarg_segment_size: 88
    .language:       OpenCL C
    .language_version:
      - 2
      - 0
    .max_flat_workgroup_size: 1024
    .name:           _Z5k_csrPKiS0_PiS1_PKfS3_S3_S3_PDF16_P15HIP_vector_typeIfLj4EES7_
    .private_segment_fixed_size: 0
    .sgpr_count:     86
    .sgpr_spill_count: 0
    .symbol:         _Z5k_csrPKiS0_PiS1_PKfS3_S3_S3_PDF16_P15HIP_vector_typeIfLj4EES7_.kd
    .uniform_work_group_size: 1
    .uses_dynamic_stack: false
    .vgpr_count:     64
    .vgpr_spill_count: 0
    .wavefront_size: 64
  - .agpr_count:     0
    .args:
      - .actual_access:  read_only
        .address_space:  global
        .offset:         0
        .size:           8
        .value_kind:     global_buffer
      - .actual_access:  write_only
        .address_space:  global
        .offset:         8
        .size:           8
        .value_kind:     global_buffer
      - .actual_access:  write_only
        .address_space:  global
        .offset:         16
        .size:           8
        .value_kind:     global_buffer
    .group_segment_fixed_size: 16
    .kernarg_segment_align: 8
    .kernarg_segment_size: 24
    .language:       OpenCL C
    .language_version:
      - 2
      - 0
    .max_flat_workgroup_size: 256
    .name:           _Z6k_pre2PKiPiS1_
    .private_segment_fixed_size: 0
    .sgpr_count:     14
    .sgpr_spill_count: 0
    .symbol:         _Z6k_pre2PKiPiS1_.kd
    .uniform_work_group_size: 1
    .uses_dynamic_stack: false
    .vgpr_count:     14
    .vgpr_spill_count: 0
    .wavefront_size: 64
  - .agpr_count:     0
    .args:
      - .actual_access:  read_only
        .address_space:  global
        .offset:         0
        .size:           8
        .value_kind:     global_buffer
      - .actual_access:  read_only
        .address_space:  global
        .offset:         8
        .size:           8
        .value_kind:     global_buffer
      - .actual_access:  read_only
        .address_space:  global
        .offset:         16
        .size:           8
        .value_kind:     global_buffer
      - .actual_access:  read_only
        .address_space:  global
        .offset:         24
        .size:           8
        .value_kind:     global_buffer
      - .actual_access:  read_only
        .address_space:  global
        .offset:         32
        .size:           8
        .value_kind:     global_buffer
      - .actual_access:  write_only
        .address_space:  global
        .offset:         40
        .size:           8
        .value_kind:     global_buffer
    .group_segment_fixed_size: 1408
    .kernarg_segment_align: 8
    .kernarg_segment_size: 48
    .language:       OpenCL C
    .language_version:
      - 2
      - 0
    .max_flat_workgroup_size: 256
    .name:           _Z7k_finalPKfS0_S0_S0_S0_Pf
    .private_segment_fixed_size: 0
    .sgpr_count:     26
    .sgpr_spill_count: 0
    .symbol:         _Z7k_finalPKfS0_S0_S0_S0_Pf.kd
    .uniform_work_group_size: 1
    .uses_dynamic_stack: false
    .vgpr_count:     96
    .vgpr_spill_count: 0
    .wavefront_size: 64
  - .agpr_count:     0
    .args:
      - .actual_access:  read_only
        .address_space:  global
        .offset:         0
        .size:           8
        .value_kind:     global_buffer
      - .actual_access:  read_only
        .address_space:  global
        .offset:         8
        .size:           8
        .value_kind:     global_buffer
      - .actual_access:  read_only
        .address_space:  global
        .offset:         16
        .size:           8
        .value_kind:     global_buffer
      - .actual_access:  read_only
        .address_space:  global
        .offset:         24
        .size:           8
        .value_kind:     global_buffer
      - .actual_access:  read_only
        .address_space:  global
        .offset:         32
        .size:           8
        .value_kind:     global_buffer
      - .actual_access:  read_only
        .address_space:  global
        .offset:         40
        .size:           8
        .value_kind:     global_buffer
      - .actual_access:  read_only
        .address_space:  global
        .offset:         48
        .size:           8
        .value_kind:     global_buffer
      - .actual_access:  read_only
        .address_space:  global
        .offset:         56
        .size:           8
        .value_kind:     global_buffer
      - .actual_access:  write_only
        .address_space:  global
        .offset:         64
        .size:           8
        .value_kind:     global_buffer
      - .actual_access:  write_only
        .address_space:  global
        .offset:         72
        .size:           8
        .value_kind:     global_buffer
      - .actual_access:  write_only
        .address_space:  global
        .offset:         80
        .size:           8
        .value_kind:     global_buffer
      - .actual_access:  read_only
        .address_space:  global
        .offset:         88
        .size:           8
        .value_kind:     global_buffer
      - .actual_access:  read_only
        .address_space:  global
        .offset:         96
        .size:           8
        .value_kind:     global_buffer
      - .actual_access:  read_only
        .address_space:  global
        .offset:         104
        .size:           8
        .value_kind:     global_buffer
      - .actual_access:  read_only
        .address_space:  global
        .offset:         112
        .size:           8
        .value_kind:     global_buffer
      - .actual_access:  read_only
        .address_space:  global
        .offset:         120
        .size:           8
        .value_kind:     global_buffer
      - .actual_access:  read_only
        .address_space:  global
        .offset:         128
        .size:           8
        .value_kind:     global_buffer
      - .actual_access:  read_only
        .address_space:  global
        .offset:         136
        .size:           8
        .value_kind:     global_buffer
      - .actual_access:  read_only
        .address_space:  global
        .offset:         144
        .size:           8
        .value_kind:     global_buffer
    .group_segment_fixed_size: 29248
    .kernarg_segment_align: 8
    .kernarg_segment_size: 152
    .language:       OpenCL C
    .language_version:
      - 2
      - 0
    .max_flat_workgroup_size: 256
    .name:           _Z7k_layerILi0EEvPKiS1_PKfS3_PKDF16_S3_S5_S5_PDF16_P15HIP_vector_typeIfLj4EES9_S3_S3_S3_S3_S3_S3_PfSA_
    .private_segment_fixed_size: 0
    .sgpr_count:     66
    .sgpr_spill_count: 0
    .symbol:         _Z7k_layerILi0EEvPKiS1_PKfS3_PKDF16_S3_S5_S5_PDF16_P15HIP_vector_typeIfLj4EES9_S3_S3_S3_S3_S3_S3_PfSA_.kd
    .uniform_work_group_size: 1
    .uses_dynamic_stack: false
    .vgpr_count:     86
    .vgpr_spill_count: 0
    .wavefront_size: 64
  - .agpr_count:     0
    .args:
      - .actual_access:  read_only
        .address_space:  global
        .offset:         0
        .size:           8
        .value_kind:     global_buffer
      - .actual_access:  read_only
        .address_space:  global
        .offset:         8
        .size:           8
        .value_kind:     global_buffer
      - .actual_access:  read_only
        .address_space:  global
        .offset:         16
        .size:           8
        .value_kind:     global_buffer
      - .actual_access:  read_only
        .address_space:  global
        .offset:         24
        .size:           8
        .value_kind:     global_buffer
      - .actual_access:  read_only
        .address_space:  global
        .offset:         32
        .size:           8
        .value_kind:     global_buffer
      - .actual_access:  read_only
        .address_space:  global
        .offset:         40
        .size:           8
        .value_kind:     global_buffer
      - .actual_access:  read_only
        .address_space:  global
        .offset:         48
        .size:           8
        .value_kind:     global_buffer
      - .actual_access:  read_only
        .address_space:  global
        .offset:         56
        .size:           8
        .value_kind:     global_buffer
      - .actual_access:  write_only
        .address_space:  global
        .offset:         64
        .size:           8
        .value_kind:     global_buffer
      - .actual_access:  write_only
        .address_space:  global
        .offset:         72
        .size:           8
        .value_kind:     global_buffer
      - .actual_access:  write_only
        .address_space:  global
        .offset:         80
        .size:           8
        .value_kind:     global_buffer
      - .actual_access:  read_only
        .address_space:  global
        .offset:         88
        .size:           8
        .value_kind:     global_buffer
      - .actual_access:  read_only
        .address_space:  global
        .offset:         96
        .size:           8
        .value_kind:     global_buffer
      - .actual_access:  read_only
        .address_space:  global
        .offset:         104
        .size:           8
        .value_kind:     global_buffer
      - .actual_access:  read_only
        .address_space:  global
        .offset:         112
        .size:           8
        .value_kind:     global_buffer
      - .actual_access:  read_only
        .address_space:  global
        .offset:         120
        .size:           8
        .value_kind:     global_buffer
      - .actual_access:  read_only
        .address_space:  global
        .offset:         128
        .size:           8
        .value_kind:     global_buffer
      - .actual_access:  read_only
        .address_space:  global
        .offset:         136
        .size:           8
        .value_kind:     global_buffer
      - .actual_access:  read_only
        .address_space:  global
        .offset:         144
        .size:           8
        .value_kind:     global_buffer
    .group_segment_fixed_size: 21504
    .kernarg_segment_align: 8
    .kernarg_segment_size: 152
    .language:       OpenCL C
    .language_version:
      - 2
      - 0
    .max_flat_workgroup_size: 256
    .name:           _Z7k_layerILi1EEvPKiS1_PKfS3_PKDF16_S3_S5_S5_PDF16_P15HIP_vector_typeIfLj4EES9_S3_S3_S3_S3_S3_S3_PfSA_
    .private_segment_fixed_size: 0
    .sgpr_count:     70
    .sgpr_spill_count: 0
    .symbol:         _Z7k_layerILi1EEvPKiS1_PKfS3_PKDF16_S3_S5_S5_PDF16_P15HIP_vector_typeIfLj4EES9_S3_S3_S3_S3_S3_S3_PfSA_.kd
    .uniform_work_group_size: 1
    .uses_dynamic_stack: false
    .vgpr_count:     96
    .vgpr_spill_count: 0
    .wavefront_size: 64
  - .agpr_count:     0
    .args:
      - .actual_access:  read_only
        .address_space:  global
        .offset:         0
        .size:           8
        .value_kind:     global_buffer
      - .actual_access:  read_only
        .address_space:  global
        .offset:         8
        .size:           8
        .value_kind:     global_buffer
      - .actual_access:  read_only
        .address_space:  global
        .offset:         16
        .size:           8
        .value_kind:     global_buffer
      - .actual_access:  read_only
        .address_space:  global
        .offset:         24
        .size:           8
        .value_kind:     global_buffer
      - .actual_access:  read_only
        .address_space:  global
        .offset:         32
        .size:           8
        .value_kind:     global_buffer
      - .actual_access:  read_only
        .address_space:  global
        .offset:         40
        .size:           8
        .value_kind:     global_buffer
      - .actual_access:  read_only
        .address_space:  global
        .offset:         48
        .size:           8
        .value_kind:     global_buffer
      - .actual_access:  read_only
        .address_space:  global
        .offset:         56
        .size:           8
        .value_kind:     global_buffer
      - .actual_access:  read_only
        .address_space:  global
        .offset:         64
        .size:           8
        .value_kind:     global_buffer
      - .actual_access:  read_only
        .address_space:  global
        .offset:         72
        .size:           8
        .value_kind:     global_buffer
      - .actual_access:  read_only
        .address_space:  global
        .offset:         80
        .size:           8
        .value_kind:     global_buffer
      - .actual_access:  read_only
        .address_space:  global
        .offset:         88
        .size:           8
        .value_kind:     global_buffer
      - .actual_access:  read_only
        .address_space:  global
        .offset:         96
        .size:           8
        .value_kind:     global_buffer
      - .actual_access:  read_only
        .address_space:  global
        .offset:         104
        .size:           8
        .value_kind:     global_buffer
      - .actual_access:  read_only
        .address_space:  global
        .offset:         112
        .size:           8
        .value_kind:     global_buffer
      - .actual_access:  read_only
        .address_space:  global
        .offset:         120
        .size:           8
        .value_kind:     global_buffer
      - .actual_access:  read_only
        .address_space:  global
        .offset:         128
        .size:           8
        .value_kind:     global_buffer
      - .actual_access:  write_only
        .address_space:  global
        .offset:         136
        .size:           8
        .value_kind:     global_buffer
      - .address_space:  global
        .offset:         144
        .size:           8
        .value_kind:     global_buffer
    .group_segment_fixed_size: 19456
    .kernarg_segment_align: 8
    .kernarg_segment_size: 152
    .language:       OpenCL C
    .language_version:
      - 2
      - 0
    .max_flat_workgroup_size: 256
    .name:           _Z7k_layerILi2EEvPKiS1_PKfS3_PKDF16_S3_S5_S5_PDF16_P15HIP_vector_typeIfLj4EES9_S3_S3_S3_S3_S3_S3_PfSA_
    .private_segment_fixed_size: 0
    .sgpr_count:     74
    .sgpr_spill_count: 0
    .symbol:         _Z7k_layerILi2EEvPKiS1_PKfS3_PKDF16_S3_S5_S5_PDF16_P15HIP_vector_typeIfLj4EES9_S3_S3_S3_S3_S3_S3_PfSA_.kd
    .uniform_work_group_size: 1
    .uses_dynamic_stack: false
    .vgpr_count:     110
    .vgpr_spill_count: 0
    .wavefront_size: 64
